# speedup vs baseline: 1.0533x; 1.0031x over previous
_Z10agg_kernelPKDF16_PKiS2_S2_PKfS2_PDF16_Pfi:
	s_load_dwordx8 s[12:19], s[0:1], 0x0
	s_lshl_b32 s4, s2, 1
	s_ashr_i32 s5, s4, 31
	s_lshl_b64 s[4:5], s[4:5], 2
	v_and_b32_e32 v1, 63, v0
	s_waitcnt lgkmcnt(0)
	s_add_u32 s20, s16, s4
	s_addc_u32 s21, s17, s5
	s_load_dwordx2 s[16:17], s[20:21], 0x0
	s_load_dwordx8 s[4:11], s[0:1], 0x20
	v_readfirstlane_b32 s3, v0
	v_lshlrev_b32_e32 v2, 2, v1
	s_lshr_b32 s3, s3, 6
	s_waitcnt lgkmcnt(0)
	s_ashr_i32 s21, s16, 31
	s_mov_b32 s20, s16
	global_load_dword v3, v2, s[6:7]
	global_load_dword v4, v2, s[6:7] offset:256
	global_load_dword v6, v2, s[6:7] offset:512
	global_load_dword v5, v2, s[6:7] offset:768
	s_lshl_b64 s[6:7], s[20:21], 2
	s_add_u32 s6, s14, s6
	s_addc_u32 s7, s15, s7
	s_add_i32 s21, s17, 15
	s_ashr_i32 s21, s21, 4
	s_max_i32 s20, s21, 1
	s_add_i32 s20, s20, -1
	s_min_u32 s14, s3, s20
	s_bfe_u32 s44, s2, 0x10002
	s_mul_i32 s45, s44, s20
	s_lshl_b32 s44, s44, 1
	s_sub_i32 s44, 1, s44
	s_mul_i32 s14, s14, s44
	s_add_i32 s14, s14, s45
	s_lshl_b32 s30, s14, 4
	v_mov_b32_e32 v59, 0x30e0000
	v_bfe_u32 v2, v0, 4, 2
	v_lshlrev_b32_e32 v7, 2, v0
	s_lshl_b32 s14, s14, 6
	v_and_or_b32 v18, v7, 12, v2
	s_add_u32 s14, s6, s14
	s_addc_u32 s15, s7, 0
	v_lshlrev_b32_e32 v2, 2, v18
	global_load_dword v2, v2, s[14:15] nt
	v_lshlrev_b32_e32 v20, 2, v18
	v_mov_b32_e32 v8, 0
	v_or_b32_e32 v9, 0xfffffc00, v0
	s_mov_b64 s[14:15], 0
	s_movk_i32 s16, 0x762f
.LBB2_1:
	v_add_u32_e32 v9, 0x400, v9
	v_cmp_lt_u32_e32 vcc, s16, v9
	ds_write_b32 v7, v8
	s_or_b64 s[14:15], vcc, s[14:15]
	v_add_u32_e32 v7, 0x1000, v7
	s_andn2_b64 exec, exec, s[14:15]
	s_cbranch_execnz .LBB2_1
	s_or_b64 exec, exec, s[14:15]
	s_waitcnt vmcnt(2)
	v_max3_i32 v3, v3, v4, v6
	v_mbcnt_lo_u32_b32 v4, -1, 0
	v_mbcnt_hi_u32_b32 v4, -1, v4
	v_and_b32_e32 v25, 64, v4
	s_waitcnt vmcnt(1)
	v_max3_i32 v3, v3, v5, 0
	v_add_u32_e32 v5, 64, v25
	v_xor_b32_e32 v6, 1, v4
	v_cmp_lt_i32_e32 vcc, v6, v5
	s_load_dword s16, s[0:1], 0x40
	s_mul_i32 s14, s2, 0x187
	v_cndmask_b32_e32 v6, v4, v6, vcc
	v_lshlrev_b32_e32 v6, 2, v6
	ds_bpermute_b32 v6, v6, v3
	s_waitcnt lgkmcnt(0)
	s_sub_i32 s15, s16, s14
	s_movk_i32 s0, 0x73
	s_cmp_gt_i32 s21, s3
	s_cselect_b64 s[22:23], -1, 0
	v_max_i32_e32 v3, v3, v6
	v_xor_b32_e32 v6, 2, v4
	v_cmp_lt_i32_e32 vcc, v6, v5
	v_mov_b32_e32 v29, 0
	v_mov_b32_e32 v27, 0
	v_cndmask_b32_e32 v6, v4, v6, vcc
	v_lshlrev_b32_e32 v6, 2, v6
	ds_bpermute_b32 v6, v6, v3
	v_mov_b32_e32 v28, 0
	v_mov_b32_e32 v26, 0
	v_mov_b32_e32 v21, 0
	s_waitcnt vmcnt(0)
	v_add_u32_e32 v33, s30, v18
	v_cmp_gt_i32_e64 s[28:29], s17, v33
	s_nop 1
	v_cndmask_b32_e64 v2, v59, v2, s[28:29]
	s_nop 1
	v_mov_b32_dpp v29, v2 row_newbcast:0 row_mask:0xf bank_mask:0xf
	s_waitcnt lgkmcnt(0)
	v_max_i32_e32 v3, v3, v6
	v_xor_b32_e32 v6, 4, v4
	v_cmp_lt_i32_e32 vcc, v6, v5
	v_mov_b32_dpp v27, v2 row_newbcast:1 row_mask:0xf bank_mask:0xf
	v_mov_b32_dpp v28, v2 row_newbcast:2 row_mask:0xf bank_mask:0xf
	v_cndmask_b32_e32 v6, v4, v6, vcc
	v_lshlrev_b32_e32 v6, 2, v6
	ds_bpermute_b32 v6, v6, v3
	v_mov_b32_dpp v26, v2 row_newbcast:3 row_mask:0xf bank_mask:0xf
	s_waitcnt lgkmcnt(0)
	s_barrier
	v_max_i32_e32 v3, v3, v6
	v_xor_b32_e32 v6, 8, v4
	v_cmp_lt_i32_e32 vcc, v6, v5
	s_nop 1
	v_cndmask_b32_e32 v6, v4, v6, vcc
	v_lshlrev_b32_e32 v60, 2, v6
	ds_bpermute_b32 v6, v60, v3
	s_waitcnt lgkmcnt(0)
	v_max_i32_e32 v3, v3, v6
	v_xor_b32_e32 v6, 16, v4
	v_cmp_lt_i32_e32 vcc, v6, v5
	s_nop 1
	v_cndmask_b32_e32 v6, v4, v6, vcc
	v_lshlrev_b32_e32 v61, 2, v6
	ds_bpermute_b32 v6, v61, v3
	s_waitcnt lgkmcnt(0)
	v_max_i32_e32 v3, v3, v6
	v_xor_b32_e32 v6, 32, v4
	v_cmp_lt_i32_e32 vcc, v6, v5
	v_and_b32_e32 v5, 15, v0
	v_lshlrev_b32_e32 v24, 4, v5
	v_cndmask_b32_e32 v4, v4, v6, vcc
	v_lshlrev_b32_e32 v66, 2, v4
	ds_bpermute_b32 v4, v66, v3
	v_lshlrev_b32_e32 v23, 2, v5
	s_waitcnt lgkmcnt(0)
	v_max_i32_e32 v3, v3, v4
	v_lshrrev_b32_e32 v3, 23, v3
	v_mov_b32_e32 v4, 0x8b
	v_med3_u32 v3, v3, s0, v4
	s_sub_i32 s0, s21, s3
	s_add_i32 s0, s0, 15
	s_cmp_gt_u32 s0, 15
	s_cselect_b64 s[24:25], -1, 0
	v_lshlrev_b32_e32 v19, 23, v3
	s_and_b64 s[22:23], s[22:23], s[24:25]
	v_sub_u32_e32 v22, 0x84800000, v19
	s_and_b64 vcc, exec, s[22:23]
	s_cbranch_vccz .LBB2_5
	s_lshr_b32 s21, s0, 4
	s_mov_b32 s1, 0
	s_mov_b32 s22, 0x1ffff00
	s_mov_b32 s23, 0x4b400000
	v_lshl_add_u64 v[20:21], s[6:7], 0, v[20:21]
	s_add_i32 s0, s3, 16
	s_mov_b32 s24, s0
	s_min_i32 s24, s24, s20
	s_mul_i32 s24, s24, s44
	s_add_i32 s24, s24, s45
	s_lshl_b32 s24, s24, 4
	s_ashr_i32 s25, s24, 31
	v_lshl_add_u64 v[32:33], s[24:25], 2, v[20:21]
	global_load_dword v30, v[32:33], off nt
	v_lshlrev_b32_e32 v35, 8, v29
	v_and_or_b32 v35, v35, s22, v24
	global_load_dwordx4 v[2:5], v35, s[12:13]
	v_lshlrev_b32_e32 v35, 8, v27
	v_and_or_b32 v35, v35, s22, v24
	global_load_dwordx4 v[6:9], v35, s[12:13]
	v_lshlrev_b32_e32 v35, 8, v28
	v_and_or_b32 v35, v35, s22, v24
	global_load_dwordx4 v[10:13], v35, s[12:13]
	v_lshlrev_b32_e32 v35, 8, v26
	v_and_or_b32 v35, v35, s22, v24
	global_load_dwordx4 v[14:17], v35, s[12:13]
.Lagg_loop:
	s_waitcnt vmcnt(4)
	s_mov_b32 s24, s0
	s_min_i32 s24, s24, s20
	s_mul_i32 s24, s24, s44
	s_add_i32 s24, s24, s45
	s_lshl_b32 s24, s24, 4
	v_add_u32_e32 v33, s24, v18
	v_cmp_gt_i32_e64 s[28:29], s17, v33
	s_add_i32 s24, s0, 16
	s_min_i32 s24, s24, s20
	s_mul_i32 s24, s24, s44
	s_add_i32 s24, s24, s45
	s_lshl_b32 s24, s24, 4
	s_ashr_i32 s25, s24, 31
	v_cndmask_b32_e64 v31, v59, v30, s[28:29]
	v_lshl_add_u64 v[32:33], s[24:25], 2, v[20:21]
	global_load_dword v30, v[32:33], off nt
	s_waitcnt vmcnt(4)
	v_ashrrev_i32_e32 v32, 17, v29
	v_mul_i32_i24_e32 v32, 0x140, v32
	v_fma_mix_f32 v33, v2, v22, s23 op_sel_hi:[1,0,0]
	v_fma_mix_f32 v34, v2, v22, s23 op_sel:[1,0,0] op_sel_hi:[1,0,0]
	v_or_b32_e32 v32, v23, v32
	v_lshl_add_u32 v33, v34, 16, v33
	ds_add_u32 v32, v33
	v_fma_mix_f32 v33, v3, v22, s23 op_sel_hi:[1,0,0]
	v_fma_mix_f32 v34, v3, v22, s23 op_sel:[1,0,0] op_sel_hi:[1,0,0]
	s_nop 0
	v_lshl_add_u32 v33, v34, 16, v33
	ds_add_u32 v32, v33 offset:64
	v_fma_mix_f32 v33, v4, v22, s23 op_sel_hi:[1,0,0]
	v_fma_mix_f32 v34, v4, v22, s23 op_sel:[1,0,0] op_sel_hi:[1,0,0]
	s_nop 0
	v_lshl_add_u32 v33, v34, 16, v33
	ds_add_u32 v32, v33 offset:128
	v_fma_mix_f32 v33, v5, v22, s23 op_sel_hi:[1,0,0]
	v_fma_mix_f32 v34, v5, v22, s23 op_sel:[1,0,0] op_sel_hi:[1,0,0]
	s_nop 0
	v_lshl_add_u32 v33, v34, 16, v33
	ds_add_u32 v32, v33 offset:192
	v_mov_b32_e32 v29, 0
	s_nop 1
	v_mov_b32_dpp v29, v31 row_newbcast:0 row_mask:0xf bank_mask:0xf
	v_lshlrev_b32_e32 v35, 8, v29
	v_and_or_b32 v35, v35, s22, v24
	s_waitcnt vmcnt(1)
	global_load_dwordx4 v[2:5], v35, s[12:13]
	s_waitcnt vmcnt(4)
	v_ashrrev_i32_e32 v32, 17, v27
	v_mul_i32_i24_e32 v32, 0x140, v32
	v_fma_mix_f32 v33, v6, v22, s23 op_sel_hi:[1,0,0]
	v_fma_mix_f32 v34, v6, v22, s23 op_sel:[1,0,0] op_sel_hi:[1,0,0]
	v_or_b32_e32 v32, v23, v32
	v_lshl_add_u32 v33, v34, 16, v33
	ds_add_u32 v32, v33
	v_fma_mix_f32 v33, v7, v22, s23 op_sel_hi:[1,0,0]
	v_fma_mix_f32 v34, v7, v22, s23 op_sel:[1,0,0] op_sel_hi:[1,0,0]
	s_nop 0
	v_lshl_add_u32 v33, v34, 16, v33
	ds_add_u32 v32, v33 offset:64
	v_fma_mix_f32 v33, v8, v22, s23 op_sel_hi:[1,0,0]
	v_fma_mix_f32 v34, v8, v22, s23 op_sel:[1,0,0] op_sel_hi:[1,0,0]
	s_nop 0
	v_lshl_add_u32 v33, v34, 16, v33
	ds_add_u32 v32, v33 offset:128
	v_fma_mix_f32 v33, v9, v22, s23 op_sel_hi:[1,0,0]
	v_fma_mix_f32 v34, v9, v22, s23 op_sel:[1,0,0] op_sel_hi:[1,0,0]
	s_nop 0
	v_lshl_add_u32 v33, v34, 16, v33
	ds_add_u32 v32, v33 offset:192
	v_mov_b32_e32 v27, 0
	s_nop 1
	v_mov_b32_dpp v27, v31 row_newbcast:1 row_mask:0xf bank_mask:0xf
	v_lshlrev_b32_e32 v35, 8, v27
	v_and_or_b32 v35, v35, s22, v24
	s_waitcnt vmcnt(1)
	global_load_dwordx4 v[6:9], v35, s[12:13]
	s_waitcnt vmcnt(4)
	v_ashrrev_i32_e32 v32, 17, v28
	v_mul_i32_i24_e32 v32, 0x140, v32
	v_fma_mix_f32 v33, v10, v22, s23 op_sel_hi:[1,0,0]
	v_fma_mix_f32 v34, v10, v22, s23 op_sel:[1,0,0] op_sel_hi:[1,0,0]
	v_or_b32_e32 v32, v23, v32
	v_lshl_add_u32 v33, v34, 16, v33
	ds_add_u32 v32, v33
	v_fma_mix_f32 v33, v11, v22, s23 op_sel_hi:[1,0,0]
	v_fma_mix_f32 v34, v11, v22, s23 op_sel:[1,0,0] op_sel_hi:[1,0,0]
	s_nop 0
	v_lshl_add_u32 v33, v34, 16, v33
	ds_add_u32 v32, v33 offset:64
	v_fma_mix_f32 v33, v12, v22, s23 op_sel_hi:[1,0,0]
	v_fma_mix_f32 v34, v12, v22, s23 op_sel:[1,0,0] op_sel_hi:[1,0,0]
	s_nop 0
	v_lshl_add_u32 v33, v34, 16, v33
	ds_add_u32 v32, v33 offset:128
	v_fma_mix_f32 v33, v13, v22, s23 op_sel_hi:[1,0,0]
	v_fma_mix_f32 v34, v13, v22, s23 op_sel:[1,0,0] op_sel_hi:[1,0,0]
	s_nop 0
	v_lshl_add_u32 v33, v34, 16, v33
	ds_add_u32 v32, v33 offset:192
	v_mov_b32_e32 v28, 0
	s_nop 1
	v_mov_b32_dpp v28, v31 row_newbcast:2 row_mask:0xf bank_mask:0xf
	v_lshlrev_b32_e32 v35, 8, v28
	v_and_or_b32 v35, v35, s22, v24
	s_waitcnt vmcnt(1)
	global_load_dwordx4 v[10:13], v35, s[12:13]
	s_waitcnt vmcnt(4)
	v_ashrrev_i32_e32 v32, 17, v26
	v_mul_i32_i24_e32 v32, 0x140, v32
	v_fma_mix_f32 v33, v14, v22, s23 op_sel_hi:[1,0,0]
	v_fma_mix_f32 v34, v14, v22, s23 op_sel:[1,0,0] op_sel_hi:[1,0,0]
	v_or_b32_e32 v32, v23, v32
	v_lshl_add_u32 v33, v34, 16, v33
	ds_add_u32 v32, v33
	v_fma_mix_f32 v33, v15, v22, s23 op_sel_hi:[1,0,0]
	v_fma_mix_f32 v34, v15, v22, s23 op_sel:[1,0,0] op_sel_hi:[1,0,0]
	s_nop 0
	v_lshl_add_u32 v33, v34, 16, v33
	ds_add_u32 v32, v33 offset:64
	v_fma_mix_f32 v33, v16, v22, s23 op_sel_hi:[1,0,0]
	v_fma_mix_f32 v34, v16, v22, s23 op_sel:[1,0,0] op_sel_hi:[1,0,0]
	s_nop 0
	v_lshl_add_u32 v33, v34, 16, v33
	ds_add_u32 v32, v33 offset:128
	v_fma_mix_f32 v33, v17, v22, s23 op_sel_hi:[1,0,0]
	v_fma_mix_f32 v34, v17, v22, s23 op_sel:[1,0,0] op_sel_hi:[1,0,0]
	s_nop 0
	v_lshl_add_u32 v33, v34, 16, v33
	ds_add_u32 v32, v33 offset:192
	v_mov_b32_e32 v26, 0
	s_nop 1
	v_mov_b32_dpp v26, v31 row_newbcast:3 row_mask:0xf bank_mask:0xf
	v_lshlrev_b32_e32 v35, 8, v26
	v_and_or_b32 v35, v35, s22, v24
	s_waitcnt vmcnt(1)
	global_load_dwordx4 v[14:17], v35, s[12:13]
	s_add_i32 s1, s1, 1
	s_add_i32 s0, s0, 16
	s_cmp_lt_u32 s1, s21
	s_cbranch_scc1 .Lagg_loop
